# v23 + row_scale_table fast path in the w1 phase: with 256 workgroups all units share one row panel, so threads 0-255 compute the 256 rstd once (8 loads each, same summation tree) and fill units 0-3; g
# speedup vs baseline: 1.0106x; 1.0085x over previous
.LBB0_1179:
	v_readlane_b32 s8, v254, 0
	s_mov_b64 s[26:27], s[82:83]
	v_readlane_b32 s9, v254, 1
	v_mov_b32_e32 v1, v0
	s_ashr_i32 s9, s8, 31
	s_waitcnt vmcnt(0)
	s_cmp_lg_u32 s33, 0x100
	s_cbranch_scc1 .Lrst_w1_slow
	v_cmp_gt_u32_e32 vcc, 0x100, v0
	s_and_saveexec_b64 s[0:1], vcc
	s_cbranch_execz .Lrst_w1_done
	s_and_b32 s7, s8, 7
	s_lshl_b32 s7, s7, 2
	s_bfe_u32 s10, s8, 0x20003
	s_or_b32 s7, s7, s10
	s_lshl_b32 s7, s7, 15
	s_add_u32 s10, s82, 0x36300000
	s_addc_u32 s11, s83, 0
	s_add_u32 s10, s10, s7
	s_addc_u32 s11, s11, 0
	v_lshlrev_b32_e32 v2, 7, v0
	global_load_dwordx4 v[4:7], v2, s[10:11]
	global_load_dwordx4 v[8:11], v2, s[10:11] offset:16
	global_load_dwordx4 v[12:15], v2, s[10:11] offset:32
	global_load_dwordx4 v[16:19], v2, s[10:11] offset:48
	global_load_dwordx4 v[20:23], v2, s[10:11] offset:64
	global_load_dwordx4 v[24:27], v2, s[10:11] offset:80
	global_load_dwordx4 v[28:31], v2, s[10:11] offset:96
	global_load_dwordx4 v[32:35], v2, s[10:11] offset:112
	v_readlane_b32 s7, v255, 4
	v_mov_b32_e32 v36, 0x358637bd
	s_waitcnt vmcnt(0)
	v_pk_add_f32 v[4:5], v[4:5], v[8:9]
	v_pk_add_f32 v[6:7], v[6:7], v[10:11]
	v_pk_add_f32 v[12:13], v[12:13], v[16:17]
	v_pk_add_f32 v[14:15], v[14:15], v[18:19]
	v_pk_add_f32 v[20:21], v[20:21], v[24:25]
	v_pk_add_f32 v[22:23], v[22:23], v[26:27]
	v_pk_add_f32 v[28:29], v[28:29], v[32:33]
	v_pk_add_f32 v[30:31], v[30:31], v[34:35]
	v_pk_add_f32 v[4:5], v[4:5], v[12:13]
	v_pk_add_f32 v[6:7], v[6:7], v[14:15]
	v_pk_add_f32 v[20:21], v[20:21], v[28:29]
	v_pk_add_f32 v[22:23], v[22:23], v[30:31]
	v_pk_add_f32 v[4:5], v[4:5], v[20:21]
	v_pk_add_f32 v[6:7], v[6:7], v[22:23]
	s_nop 0
	v_add_f32_e32 v4, v5, v4
	v_add_f32_e32 v6, v6, v7
	v_add_f32_e32 v4, v4, v6
	v_fmamk_f32 v4, v4, 0x3a000000, v36
	v_rsq_f32_e32 v4, v4
	v_lshl_add_u32 v3, v0, 2, s7
	s_nop 0
	ds_write_b32 v3, v4
	ds_write_b32 v3, v4 offset:1024
	ds_write_b32 v3, v4 offset:2048
	ds_write_b32 v3, v4 offset:3072
.Lrst_w1_done:
	s_or_b64 exec, exec, s[0:1]
	s_branch .LBB0_1213
.Lrst_w1_slow:
	v_mov_b64_e32 v[2:3], s[8:9]
	v_ashrrev_i32_e32 v34, 8, v1
	v_mad_i64_i32 v[2:3], s[0:1], v34, s33, v[2:3]
	s_mov_b64 s[0:1], 0x400
	s_nop 0
	v_cmp_gt_i64_e32 vcc, s[0:1], v[2:3]
	v_mov_b32_e32 v37, 0
	s_and_saveexec_b64 s[10:11], vcc
	s_cbranch_execz .LBB0_1185
	v_ashrrev_i32_e32 v3, 31, v2
	v_lshrrev_b32_e32 v3, 29, v3
	v_add_u32_e32 v3, v2, v3
	v_and_b32_e32 v4, -8, v3
	v_sub_u32_e32 v4, v2, v4
	v_cmp_lt_i32_e64 s[0:1], -1, v4
	s_and_saveexec_b64 s[12:13], s[0:1]
	s_xor_b64 s[0:1], exec, s[12:13]
	v_lshlrev_b32_e32 v2, 7, v4
	s_andn2_saveexec_b64 s[0:1], s[0:1]
	v_lshl_add_u32 v2, v4, 7, v4
	s_or_b64 exec, exec, s[0:1]
	v_ashrrev_i32_e32 v3, 3, v3
	v_add_u32_e32 v2, v2, v3
	v_ashrrev_i32_e32 v3, 31, v2
	v_lshrrev_b32_e32 v3, 25, v3
	v_add_u32_e32 v3, v2, v3
	v_ashrrev_i32_e32 v4, 7, v3
	v_lshlrev_b32_e32 v4, 2, v4
	v_sub_u32_e32 v5, 32, v4
	v_min_i32_e32 v5, 4, v5
	s_waitcnt lgkmcnt(3)
	v_sub_u32_e32 v6, 0, v5
	v_max_i32_e32 v5, v5, v6
	v_cvt_f32_u32_e32 v6, v5
	v_and_b32_e32 v3, 0xffffff80, v3
	v_sub_u32_e32 v2, v2, v3
	s_waitcnt lgkmcnt(2)
	v_sub_u32_e32 v7, 0, v2
	v_rcp_iflag_f32_e32 v6, v6
	v_ashrrev_i32_e32 v3, 31, v2
	v_max_i32_e32 v2, v2, v7
	v_sub_u32_e32 v7, 0, v5
	v_mul_f32_e32 v6, 0x4f7ffffe, v6
	v_cvt_u32_f32_e32 v6, v6
	v_mul_lo_u32 v7, v7, v6
	v_mul_hi_u32 v7, v6, v7
	v_add_u32_e32 v6, v6, v7
	v_mul_hi_u32 v6, v2, v6
	v_mul_lo_u32 v6, v6, v5
	v_sub_u32_e32 v2, v2, v6
	v_sub_u32_e32 v6, v2, v5
	v_cmp_ge_u32_e64 s[0:1], v2, v5
	s_nop 1
	v_cndmask_b32_e64 v2, v2, v6, s[0:1]
	v_sub_u32_e32 v6, v2, v5
	v_cmp_ge_u32_e64 s[0:1], v2, v5
	s_nop 1
	v_cndmask_b32_e64 v2, v2, v6, s[0:1]
	v_xor_b32_e32 v2, v2, v3
	v_sub_u32_e32 v2, v2, v3
	v_add_u32_e32 v37, v4, v2
